# static s_setprio 1 for waves 4-7 during the attention phase (strategy: one static priority raise for the younger half)
# baseline (speedup 1.0000x reference)
; #define MKCTX() const Ctx P{InTbl{in_tbl()}, (float*)*(__attribute__((address_space(1))) float* const*)((const char*)in_tbl() + offsetof(Params, out)), ws}
; #define IN(k) (((PH_MASK >> (k)) & 1) && KARG_I(ph_lo) <= (k) && (k) < KARG_I(ph_hi))
; __global__ void __launch_bounds__(512, 2) fwd_kernel(Params KP) {
;     ...
;     if (IN(11)) { MKCTX();
;         const unsigned char* Qb = ws + WS_Q; const unsigned char* Kb = ws + WS_K; const unsigned char* Vb = ws + WS_V; bf16_t* CAT = (bf16_t*)(ws + WS_Y0);
;         for (int rp = 0; rp < REPS(11); ++rp)
;         for (int un = vcu; un < NB * 8 * 16; un += G) {
;             const int qb = un & 15, bh = un >> 4, h = bh & 7, b = bh >> 3;
;             __syncthreads();
;             att::attn_body(Qb + ((size_t)(b * SEQ + qb * 256) * 1536 + h * 192), Kb + ((size_t)b * KVL * 1536 + h * 192), Vb + (size_t)(b * 8 + h) * 128 * KVL,
.LBB0_2152:
	s_or_b64 exec, exec, s[40:41]
	s_mov_b64 s[2:3], s[0:1]
	s_nop 0
	v_mov_b64_e32 v[2:3], s[2:3]
	flat_load_dword v1, v[2:3] offset:296
	s_waitcnt vmcnt(0) lgkmcnt(0)
	v_cmp_gt_i32_e32 vcc, 12, v1
	s_and_saveexec_b64 s[4:5], vcc
	s_cbranch_execz .LBB0_2180
	s_mov_b64 s[2:3], s[0:1]
	s_nop 0
	v_mov_b64_e32 v[2:3], s[2:3]
	flat_load_dword v1, v[2:3] offset:300
	s_waitcnt vmcnt(0) lgkmcnt(0)
	v_cmp_lt_i32_e32 vcc, 11, v1
	s_and_b64 exec, exec, vcc
	s_cbranch_execz .LBB0_2180
	v_readfirstlane_b32 s98, v0
	s_nop 3
	s_lshr_b32 s98, s98, 6
	s_cmp_ge_u32 s98, 4
	s_cbranch_scc0 .Lattn_prio_done
	s_setprio 1
.Lattn_prio_done:
	s_mov_b64 s[2:3], s[0:1]
	s_mov_b64 s[2:3], s[0:1]
	s_cmpk_gt_i32 s33, 0x1ff
	s_cbranch_scc1 .LBB0_2180
	s_add_u32 s9, s36, 0x333c0000
	s_addc_u32 s20, s37, 0
	s_add_u32 s21, s36, 0x363c0000
	s_addc_u32 s22, s37, 0
	s_add_u32 s23, s36, 0x396c0000
	s_addc_u32 s24, s37, 0
	s_add_u32 s25, s36, 0x28ec0000
	s_addc_u32 s26, s37, 0
	s_add_u32 s27, s36, 0x36408000
	s_addc_u32 s28, s37, 0
	s_movk_i32 s29, 0x600
	s_mov_b32 s7, 0
	s_add_i32 s30, 0, 0x11400
	s_movk_i32 s31, 0xffe0
	v_mov_b32_e32 v163, 0
	s_movk_i32 s34, 0x1100
	s_movk_i32 s35, 0x50
	s_movk_i32 s38, 0x100
	s_mov_b32 s40, 0x2aaaaaab
	s_movk_i32 s41, 0xfad0
	s_add_i32 s42, 0, 0x7800
	s_mov_b64 s[10:11], 0x30000
	s_mov_b32 s43, 0x41000000
	v_mov_b32_e32 v1, 0xf149f2ca
	s_mov_b32 s44, s33
	s_branch .LBB0_2157

; __device__ __forceinline__ void xcd_barrier(const XcdBarrier& b) {
;     asm volatile("s_waitcnt vmcnt(0)" ::: "memory");
;     __syncthreads();
;     int t_ = threadIdx.x; asm volatile("" : "+v"(t_));
;     if (t_ == 0) {
;         unsigned* bar = b.bar;
;         __builtin_amdgcn_s_waitcnt(0);
;         unsigned nloc = b.st[0], nx = b.st[1];
;         if (nloc == 0u) { xcd_barrier_complete(bar, b.x, b.G, nloc, nx); b.st[0] = nloc; b.st[1] = nx; }
.LBB0_2180:
	s_or_b64 exec, exec, s[4:5]
	s_setprio 0
	s_mov_b64 s[2:3], s[0:1]
	s_nop 0
	v_mov_b64_e32 v[2:3], s[2:3]
	flat_load_dword v1, v[2:3] offset:296
	s_waitcnt vmcnt(0) lgkmcnt(0)
	v_cmp_gt_i32_e32 vcc, 12, v1
	s_and_saveexec_b64 s[40:41], vcc
	s_cbranch_execz .LBB0_2238
	s_mov_b64 s[2:3], s[0:1]
	s_nop 0
	v_mov_b64_e32 v[2:3], s[2:3]
	flat_load_dword v1, v[2:3] offset:300
	s_waitcnt vmcnt(0) lgkmcnt(0)
	v_cmp_lt_i32_e32 vcc, 11, v1
	s_and_b64 exec, exec, vcc
	s_cbranch_execz .LBB0_2238
	s_mov_b64 s[2:3], s[0:1]
	s_nop 0
	v_mov_b64_e32 v[2:3], s[2:3]
	flat_load_dword v1, v[2:3] offset:296
	s_waitcnt vmcnt(0) lgkmcnt(0)
	v_cmp_gt_i32_e32 vcc, 13, v1
	s_and_b64 exec, exec, vcc
	s_cbranch_execz .LBB0_2238
	s_mov_b64 s[2:3], s[0:1]
	s_nop 0
	v_mov_b64_e32 v[2:3], s[2:3]
	flat_load_dword v1, v[2:3] offset:300
	s_waitcnt vmcnt(0) lgkmcnt(0)
	v_cmp_lt_i32_e32 vcc, 12, v1
	s_and_b64 exec, exec, vcc
	s_cbranch_execz .LBB0_2238
	s_mov_b64 s[4:5], s[0:1]
	s_getreg_b32 s2, hwreg(HW_REG_XCC_ID, 0, 4)
	v_mov_b32_e32 v1, v0
	v_mov_b64_e32 v[2:3], s[4:5]
	flat_load_dword v17, v[2:3] offset:308
	s_waitcnt vmcnt(0)
	s_waitcnt lgkmcnt(0)
	s_barrier
	s_nop 0
	v_cmp_eq_u32_e32 vcc, 0, v1
	s_and_b64 exec, exec, vcc
	s_cbranch_execz .LBB0_2237
	s_add_i32 s3, 0, 0x20020
	v_mov_b32_e32 v1, s3
	s_waitcnt vmcnt(0) expcnt(0) lgkmcnt(0)
	ds_read_b32 v4, v1
	s_add_i32 s3, 0, 0x20024
	v_mov_b32_e32 v1, s3
	ds_read_b32 v2, v1
	s_and_b32 s9, s2, 15
	s_waitcnt lgkmcnt(1)
	v_cmp_ne_u32_e32 vcc, 0, v4
	s_cbranch_vccnz .LBB0_2201
	s_add_u32 s2, s36, 0x1000
	s_addc_u32 s3, s37, 0
	s_add_u32 s4, s36, 0x1100
	s_addc_u32 s5, s37, 0
	s_add_u32 s6, s36, 0x1200
	s_addc_u32 s7, s37, 0
	s_add_u32 s10, s36, 0x1300
	s_addc_u32 s11, s37, 0
	s_mov_b32 s28, 1
	s_mov_b64 s[12:13], 0
	v_mov_b32_e32 v18, 0
	s_branch .LBB0_2189
